# three tail-fill sites: in-proj (6), L0 down-GEMM (5), L0 router phase beside ctx out-projection (6); attention quotas 16/18
# speedup vs baseline: 1.0027x; 1.0027x over previous
; #define LAS __attribute__((address_space(3)))
; __global__ void __launch_bounds__(512, 2) mk_fwd(Args a) {
;     extern __shared__ __attribute__((aligned(16))) unsigned char lds_raw[];
;     Ctx c; c.lds = (LAS unsigned char*)lds_raw; c.tid = threadIdx.x; c.lane = c.tid & 63; c.wave = __builtin_amdgcn_readfirstlane(c.tid >> 6); c.bid = blockIdx.x; c.G = gridDim.x;
;     volatile LAS unsigned* MISC = (volatile LAS unsigned*)(c.lds + LDS_MISC);
;     if (c.tid < 32) MISC[c.tid] = 0u;
;     __syncthreads();
;     XcdBarrier bar; bar.bar = (unsigned*)(a.ws + WS_CTL) + 4096; bar.x = 0; bar.st = nullptr;
;     const int lo = a.ph_lo, hi = a.ph_hi;
;     if (hi - lo > 1) bar = xcd_barrier_post((unsigned*)(a.ws + WS_CTL) + 4096, MISC + 8);
_Z6mk_fwd4Args:
	v_writelane_b32 v255, 0, 44
	v_writelane_b32 v255, 0, 43
	v_writelane_b32 v255, 0, 42
	s_mov_b64 s[36:37], s[0:1]
	s_load_dword s91, s[0:1], 0xf0
	s_add_u32 s0, s36, 0xf0
	s_addc_u32 s1, s37, 0
	s_mov_b32 s90, s2
	v_writelane_b32 v252, s0, 0
	v_cmp_gt_u32_e32 vcc, 32, v0
	s_nop 0
	v_writelane_b32 v252, s1, 1
	s_and_saveexec_b64 s[0:1], vcc
	v_lshl_add_u32 v1, v0, 2, 0
	v_add_u32_e32 v1, 0x27000, v1
	v_mov_b32_e32 v2, 0
	ds_write_b32 v1, v2
	s_or_b64 exec, exec, s[0:1]
	s_load_dwordx4 s[68:71], s[36:37], 0xe0
	s_mov_b32 s33, 0
	v_cmp_eq_u32_e32 vcc, 0, v0
	s_waitcnt lgkmcnt(0)
	s_barrier
	s_add_u32 s0, s68, 0x4000
	s_addc_u32 s1, s69, 0
	s_sub_i32 s2, s71, s70
	v_writelane_b32 v252, s0, 2
	s_cmp_gt_i32 s2, 1
	s_nop 0
	v_writelane_b32 v252, s1, 3
	s_cselect_b64 s[0:1], -1, 0
	s_cmp_lt_i32 s2, 2
	s_mov_b32 s2, 0
	v_writelane_b32 v252, s2, 4
	s_cbranch_scc1 .LBB0_8
	s_getreg_b32 s2, hwreg(HW_REG_XCC_ID, 0, 4)
	s_and_b32 s33, s2, 15
	s_and_saveexec_b64 s[2:3], vcc
	s_cbranch_execz .LBB0_7
	s_mov_b64 s[6:7], exec
	v_mbcnt_lo_u32_b32 v1, s6, 0
	v_mbcnt_hi_u32_b32 v1, s7, v1
	v_cmp_eq_u32_e32 vcc, 0, v1
	s_and_saveexec_b64 s[4:5], vcc
	s_cbranch_execz .LBB0_6
	s_bcnt1_i32_b64 s6, s[6:7]
	s_lshl_b32 s8, s33, 8
	v_mov_b32_e32 v3, s6
	v_readlane_b32 s6, v252, 2
	v_mov_b32_e32 v2, s8
	v_readlane_b32 s7, v252, 3
	s_nop 4
	global_atomic_add v2, v2, v3, s[6:7] offset:1024 sc0

; __global__ void __launch_bounds__(512, 2) mk_fwd(Args a) {
;     ...
;         if (IN(pb + 5) && (c.bid & 1) == 0) { if (l == 0) mod_items(a, c, 1); bg_take(a, c, l == 0 ? 26 : 24); }
;         if (EN(5) && IN(pb + 5)) for (int rep = 0; rep < NREP(5); ++rep) { phase_attn(a, c, l, last); }
;         if (IN(pb + 5) && (c.bid & 1) == 1) { bg_take(a, c, l == 0 ? 26 : 24); if (l == 0) mod_items(a, c, 1); }
.LBB0_1254:
	s_cmp_lt_u32 s14, 25
	s_cbranch_scc1 .Lbal1_l1
	s_mov_b32 s14, 16
	s_cmp_lt_u32 s90, 32
	s_cbranch_scc0 .Lbal1_b
	s_add_i32 s14, s14, -4

; #define GAS __attribute__((address_space(1)))
; #define WSW(T, off, l) WSP(T, WS_WSET + (size_t)(l) * WSET_STRIDE + (off))
; __device__ __forceinline__ void bg_take(const Args& a, const Ctx& c0, int n) {
;     ...
;         __syncthreads();
;     }
;     __syncthreads();
; __global__ void __launch_bounds__(512, 2) mk_fwd(Args a) {
;     ...
;         if (EN(7) && IN(pb + 7)) for (int rep = 0; rep < NREP(7); ++rep) {
;             const bool split = !last && c.G >= 64;
;             if (split && c.bid < 32) {
;                 GAS unsigned char* wsb = (GAS unsigned char*)a.ws; asm volatile("" : "+s"(wsb));
;                 ProbMixer p; p.K = DM; p.lda = DM; p.ldb = DM; p.ord.init(NC / 256, DM / 256, 32, c.bid); p.pm0 = NL / 256; p.A = (const char*)WSP(bf16, WS_Y); p.Bt = (const char*)WSW(bf16, W_OUT, l);
;                 p.xl = l == 0 ? INP(0) : nullptr; p.xc = l == 0 ? INP(2) : nullptr; p.x1 = WSP(const bf16, WS_X1); p.XM = WSP(bf16, WS_XM); p.modv = WSP(const float, WS_MODV) + (size_t)l * 5 * NMODW;
;                 pg8::gemm_phase(c.lds, p);
;                 asm volatile("s_waitcnt vmcnt(0)" ::: "memory"); __syncthreads();
;                 if (threadIdx.x == 0) { __builtin_amdgcn_fence(__ATOMIC_RELEASE, "agent"); __hip_atomic_fetch_add(WSP(unsigned, WS_CTL) + CW_CTXMIX, 1u, __ATOMIC_RELAXED, __HIP_MEMORY_SCOPE_AGENT); }
;             } else phase_router(a, c, l, last, split ? 32 : 0); }
.Lbt1_notB:
	v_readlane_b32 s2, v255, 44
	s_nop 3
	s_cmp_eq_u32 s2, 1
	s_cbranch_scc0 .Lbt1_notC
	v_writelane_b32 v255, 2, 44
	s_branch .Ltramp_backC

; __global__ void __launch_bounds__(512, 2) mk_fwd(Args a) {
;     ...
;         if (IN(pb + 5) && (c.bid & 1) == 0) { if (l == 0) mod_items(a, c, 1); bg_take(a, c, l == 0 ? 26 : 24); }
;         if (EN(5) && IN(pb + 5)) for (int rep = 0; rep < NREP(5); ++rep) { phase_attn(a, c, l, last); }
;         if (IN(pb + 5) && (c.bid & 1) == 1) { bg_take(a, c, l == 0 ? 26 : 24); if (l == 0) mod_items(a, c, 1); }
.LBB0_1493:
	v_readlane_b32 s2, v252, 54
	v_readlane_b32 s3, v252, 55
	s_andn2_b64 vcc, exec, s[2:3]
	s_cbranch_vccnz .LBB0_1700
	v_readlane_b32 s2, v254, 54
	v_readlane_b32 s3, v254, 55
	s_and_b64 s[2:3], s[2:3], exec
	v_mov_b32_e32 v1, v0
	v_readlane_b32 s4, v254, 21
	v_readlane_b32 s5, v254, 22
	v_readfirstlane_b32 s2, v1
	v_readlane_b32 s6, v254, 23
	v_readlane_b32 s7, v254, 24
	s_cselect_b32 s10, 26, 24
	s_cmp_lt_u32 s10, 25
	s_cbranch_scc1 .Lbal2_l1
	s_mov_b32 s10, 16
	s_cmp_lt_u32 s90, 32
	s_cbranch_scc0 .Lbal2_b
	s_add_i32 s10, s10, -4

; #define GAS __attribute__((address_space(1)))
; #define WSW(T, off, l) WSP(T, WS_WSET + (size_t)(l) * WSET_STRIDE + (off))
; __global__ void __launch_bounds__(512, 2) mk_fwd(Args a) {
;     ...
;         if (EN(7) && IN(pb + 7)) for (int rep = 0; rep < NREP(7); ++rep) {
;             const bool split = !last && c.G >= 64;
;             if (split && c.bid < 32) {
;                 GAS unsigned char* wsb = (GAS unsigned char*)a.ws; asm volatile("" : "+s"(wsb));
;                 ProbMixer p; p.K = DM; p.lda = DM; p.ldb = DM; p.ord.init(NC / 256, DM / 256, 32, c.bid); p.pm0 = NL / 256; p.A = (const char*)WSP(bf16, WS_Y); p.Bt = (const char*)WSW(bf16, W_OUT, l);
;                 p.xl = l == 0 ? INP(0) : nullptr; p.xc = l == 0 ? INP(2) : nullptr; p.x1 = WSP(const bf16, WS_X1); p.XM = WSP(bf16, WS_XM); p.modv = WSP(const float, WS_MODV) + (size_t)l * 5 * NMODW;
;                 pg8::gemm_phase(c.lds, p);
;                 asm volatile("s_waitcnt vmcnt(0)" ::: "memory"); __syncthreads();
;                 if (threadIdx.x == 0) { __builtin_amdgcn_fence(__ATOMIC_RELEASE, "agent"); __hip_atomic_fetch_add(WSP(unsigned, WS_CTL) + CW_CTXMIX, 1u, __ATOMIC_RELAXED, __HIP_MEMORY_SCOPE_AGENT); }
;             } else phase_router(a, c, l, last, split ? 32 : 0); }
.LBB0_2029:
	s_or_b64 exec, exec, s[4:5]
.LtailC_reload:
	v_readlane_b32 s48, v254, 35
	v_readlane_b32 s49, v254, 36
	v_readlane_b32 s50, v254, 37
	v_readlane_b32 s51, v254, 38
	v_readlane_b32 s52, v254, 39
	v_readlane_b32 s53, v254, 40
	v_readlane_b32 s54, v254, 41
	v_readlane_b32 s55, v254, 42
	v_readlane_b32 s58, v254, 45
	v_readlane_b32 s59, v254, 46
	v_readlane_b32 s60, v254, 47
	v_readlane_b32 s61, v254, 48
	v_readlane_b32 s62, v254, 49
	v_readlane_b32 s63, v254, 50
	v_readlane_b32 s56, v254, 43
	v_readlane_b32 s57, v254, 44
.LBB0_2030:
	v_readlane_b32 s2, v255, 44
	s_nop 3
	s_cmp_lg_u32 s2, 0
	s_cbranch_scc1 .LtailC_ret
	s_cmp_lt_u32 s90, 32
	s_cbranch_scc1 .LtailC_cont
	v_readlane_b32 s3, v254, 17
	s_nop 3
	s_cmp_lg_u32 s3, 0
	s_cbranch_scc1 .LtailC_cont
	s_cmp_lt_u32 s90, 160
	s_cbranch_scc1 .LtailC_go
	s_cmp_lt_u32 s90, 224
	s_cbranch_scc1 .LtailC_cont
.LtailC_go:
	v_writelane_b32 v255, 1, 44
	s_mov_b32 s30, 0xc3e00000
	s_movk_i32 s78, 0x315c
	v_readlane_b32 s76, v254, 53
	s_mov_b32 s81, 0x10000
	s_mov_b32 s82, 0x18000
	s_mov_b32 s83, 0x8000
	s_mov_b32 s86, 0xc000
	s_mov_b32 s14, 6
	s_branch .Ltramp_fwd
.LtailC_ret:
	v_writelane_b32 v255, 0, 44
	s_mov_b64 s[20:21], 0x2000
